# P4 expert-weight conversion (conversion-first workgroups): next-tile loads stay in flight across the transpose/write-out (path-specific counted vmcnt instead of the merged-path drains), slab loads iss
# speedup vs baseline: 1.0245x; 1.0131x over previous
; #define CQ_LOAD(buf, slab, src, ldw) do { _Pragma("unroll") for (int r_ = 0; r_ < 4; ++r_) a[buf][r_] = __builtin_nontemporal_load((const f32x4*)(src + (size_t)((slab) * 32 + r_) * ldw)); } while (0)
; __device__ __forceinline__ void conv_queue(const P& p, LAS unsigned char* lds, int* ctr, int max_tiles) {
;     ...
;     for (int it = 0;; ++it) {
;         const bool more = t_nxt < NMT, cur_w1 = t_cur < NM1;
;         if (tid == 0) qs[1 + (it & 1)] = (more && CQ_CAN) ? atomicAdd(ctr, 1) : NMT;
;         ++pulled;
;     ...
;         CQ_LOAD(2, 2, s1, l1); CQ_LOAD(3, 3, s1, l1);
.LBB0_818:
	s_mov_b32 s98, 0
	v_mov_b32_e32 v18, s11
	ds_read_b32 v18, v18
	s_waitcnt lgkmcnt(0)
	v_readfirstlane_b32 s25, v18
	s_cmpk_lt_i32 s25, 0x3000
	s_cselect_b64 s[10:11], -1, 0
	v_cndmask_b32_e64 v18, 0, 1, s[10:11]
	v_cmp_ne_u32_e64 s[4:5], 1, v18
	s_mov_b64 s[6:7], exec
	v_readlane_b32 s12, v242, 31
	v_readlane_b32 s13, v242, 32
	s_and_b64 s[12:13], s[6:7], s[12:13]
	s_mov_b64 exec, s[12:13]
	s_cbranch_execz .LBB0_824
	s_and_b64 vcc, exec, s[4:5]
	v_mov_b32_e32 v18, 0x3000
	s_cbranch_vccnz .LBB0_823
	s_mov_b64 s[14:15], exec
	v_mbcnt_lo_u32_b32 v18, s14, 0
	v_mbcnt_hi_u32_b32 v18, s15, v18
	v_cmp_eq_u32_e32 vcc, 0, v18
	s_and_saveexec_b64 s[12:13], vcc
	s_cbranch_execz .LBB0_822
	s_bcnt1_i32_b64 s8, s[14:15]
	v_mov_b32_e32 v73, s8
	global_atomic_add v73, v19, v73, s[0:1] sc0

; #define CQ_LOAD(buf, slab, src, ldw) do { _Pragma("unroll") for (int r_ = 0; r_ < 4; ++r_) a[buf][r_] = __builtin_nontemporal_load((const f32x4*)(src + (size_t)((slab) * 32 + r_) * ldw)); } while (0)
; __device__ __forceinline__ void conv_queue(const P& p, LAS unsigned char* lds, int* ctr, int max_tiles) {
;     ...
;     { CQ_SRC(t_cur, s0, l0); CQ_LOAD(0, 0, s0, l0); CQ_LOAD(1, 1, s0, l0); CQ_LOAD(2, 2, s0, l0); CQ_LOAD(3, 3, s0, l0); }
;     for (int it = 0;; ++it) {
;         const bool more = t_nxt < NMT, cur_w1 = t_cur < NM1;
;         if (tid == 0) qs[1 + (it & 1)] = (more && CQ_CAN) ? atomicAdd(ctr, 1) : NMT;
;         ++pulled;
;         CQ_PUT(0, 0); CQ_PUT(1, 1);
.LBB0_824:
	s_or_b64 exec, exec, s[6:7]
	global_load_dwordx4 v[52:55], v[2:3], off nt
	global_load_dwordx4 v[56:59], v[4:5], off nt
	global_load_dwordx4 v[60:63], v[6:7], off nt
	global_load_dwordx4 v[64:67], v[8:9], off nt
	global_load_dwordx4 v[2:5], v[10:11], off nt
	global_load_dwordx4 v[6:9], v[12:13], off nt
	global_load_dwordx4 v[10:13], v[14:15], off nt
	s_nop 0
	global_load_dwordx4 v[14:17], v[16:17], off nt
	s_cmpk_lt_i32 s26, 0x2000
	s_cselect_b64 s[16:17], -1, 0
	s_cmpk_gt_i32 s26, 0x1fff
	s_cselect_b64 s[14:15], -1, 0
	s_mov_b64 s[6:7], -1
	s_and_b64 vcc, exec, s[16:17]
	v_add_u32_e32 v18, 0x4000, v82
	s_cbranch_vccnz .LBB0_826
	v_mov_b32_e32 v73, v19
	v_mov_b32_e32 v74, v19
	s_waitcnt vmcnt(14)
	v_cvt_scalef32_pk_fp8_f32 v73, v20, v24, s23
	v_cvt_scalef32_pk_fp8_f32 v74, v21, v25, s23
	s_waitcnt vmcnt(12)
	v_cvt_scalef32_pk_fp8_f32 v73, v28, v32, s23 op_sel:[0,0,0,1]
	v_cvt_scalef32_pk_fp8_f32 v74, v29, v33, s23 op_sel:[0,0,0,1]
	ds_write2_b32 v18, v73, v74 offset1:33
	v_mov_b32_e32 v73, v19
	v_mov_b32_e32 v74, v19
	v_cvt_scalef32_pk_fp8_f32 v73, v22, v26, s23
	v_cvt_scalef32_pk_fp8_f32 v74, v23, v27, s23
	v_cvt_scalef32_pk_fp8_f32 v73, v30, v34, s23 op_sel:[0,0,0,1]
	v_cvt_scalef32_pk_fp8_f32 v74, v31, v35, s23 op_sel:[0,0,0,1]
	s_mov_b64 s[6:7], 0
	ds_write2_b32 v18, v73, v74 offset0:66 offset1:99

; #define CQ_LOAD(buf, slab, src, ldw) do { _Pragma("unroll") for (int r_ = 0; r_ < 4; ++r_) a[buf][r_] = __builtin_nontemporal_load((const f32x4*)(src + (size_t)((slab) * 32 + r_) * ldw)); } while (0)
; __device__ __forceinline__ void conv_queue(const P& p, LAS unsigned char* lds, int* ctr, int max_tiles) {
;     ...
;         CQ_SRC(t_nxt < NMT ? t_nxt : 0, s1, l1);
;         if (more) { CQ_LOAD(0, 0, s1, l1); CQ_LOAD(1, 1, s1, l1); }
.LBB0_835:
	s_ashr_i32 s30, s8, s29
	s_and_b32 s19, s8, s27
	s_ashr_i32 s31, s30, 31
	s_lshr_b32 s11, s19, s11
	s_and_b32 s8, s8, s28
	s_lshl_b64 s[18:19], s[30:31], s18
	s_add_u32 s12, s12, s18
	v_lshl_or_b32 v73, s11, 7, v1
	s_addc_u32 s13, s13, s19
	v_mul_hi_u32_u24_e32 v75, s10, v73
	v_mul_u32_u24_e32 v74, s10, v73
	v_lshl_add_u64 v[74:75], v[74:75], 2, s[12:13]
	s_lshl_b32 s8, s8, 10
	v_lshl_add_u64 v[74:75], v[74:75], 0, s[8:9]
	v_mov_b32_e32 v73, v19
	v_lshl_add_u64 v[74:75], v[74:75], 0, v[72:73]
	s_and_b64 vcc, exec, s[4:5]
	s_mul_i32 s12, s10, 0x74
	s_cbranch_vccnz .LBB0_841
	s_mov_b32 s98, 1
	s_lshl_b32 s8, s10, 2
	s_waitcnt vmcnt(13)
	v_lshl_add_u64 v[28:29], v[74:75], 0, s[8:9]
	global_load_dwordx4 v[20:23], v[74:75], off nt
	global_load_dwordx4 v[24:27], v[28:29], off nt
	v_lshl_add_u64 v[28:29], v[28:29], 0, s[8:9]
	s_waitcnt vmcnt(13)
	v_lshl_add_u64 v[36:37], v[28:29], 0, s[8:9]
	s_mov_b32 s13, s9
	global_load_dwordx4 v[28:31], v[28:29], off nt
	s_nop 0
	global_load_dwordx4 v[32:35], v[36:37], off nt
	v_lshl_add_u64 v[36:37], v[36:37], 0, s[12:13]
	s_waitcnt vmcnt(13)
	v_lshl_add_u64 v[44:45], v[36:37], 0, s[8:9]
	s_waitcnt vmcnt(12)
	v_lshl_add_u64 v[48:49], v[44:45], 0, s[8:9]
	global_load_dwordx4 v[36:39], v[36:37], off nt
	s_nop 0
	global_load_dwordx4 v[40:43], v[44:45], off nt
	s_nop 0
	global_load_dwordx4 v[44:47], v[48:49], off nt
	v_lshl_add_u64 v[48:49], v[48:49], 0, s[8:9]
	global_load_dwordx4 v[48:51], v[48:49], off nt
	s_and_b64 vcc, exec, s[6:7]
	s_mov_b64 s[18:19], -1
	s_cbranch_vccz .LBB0_842

; __device__ __forceinline__ void conv_queue(const P& p, LAS unsigned char* lds, int* ctr, int max_tiles) {
;     ...
;         CQ_PUT(2, 2); CQ_PUT(3, 3);
.LBB0_838:
	s_cmp_eq_u32 s98, 0
	s_cbranch_scc1 .Lcqw_0p0_a
	s_waitcnt vmcnt(14)
	s_branch .Lcqw_0p0_b

; __device__ __forceinline__ void conv_queue(const P& p, LAS unsigned char* lds, int* ctr, int max_tiles) {
;     ...
;         CQ_PUT(2, 2); CQ_PUT(3, 3);
.Lcqw_0p0_b:
	v_cvt_pk_bf16_f32 v86, v52, v56
	s_cmp_eq_u32 s98, 0
	s_cbranch_scc1 .Lcqw_0p1_a
	s_waitcnt vmcnt(12)
	s_branch .Lcqw_0p1_b

; __device__ __forceinline__ void conv_queue(const P& p, LAS unsigned char* lds, int* ctr, int max_tiles) {
;     ...
;         CQ_PUT(2, 2); CQ_PUT(3, 3);
.Lcqw_0p1_b:
	v_cvt_pk_bf16_f32 v87, v60, v64
	v_cvt_pk_bf16_f32 v52, v53, v57
	v_cvt_pk_bf16_f32 v53, v61, v65
	ds_write2_b64 v84, v[86:87], v[52:53] offset0:16 offset1:49
	v_cvt_pk_bf16_f32 v52, v54, v58
	v_cvt_pk_bf16_f32 v53, v62, v66
	v_cvt_pk_bf16_f32 v54, v55, v59
	v_cvt_pk_bf16_f32 v55, v63, v67
	ds_write2_b64 v84, v[52:53], v[54:55] offset0:82 offset1:115
	s_and_b64 vcc, exec, s[6:7]
	s_mov_b64 s[6:7], -1
	s_cbranch_vccz .LBB0_844

; __device__ __forceinline__ void conv_queue(const P& p, LAS unsigned char* lds, int* ctr, int max_tiles) {
;     ...
;         CQ_PUT(2, 2); CQ_PUT(3, 3);
.LBB0_840:
	s_cmp_eq_u32 s98, 0
	s_cbranch_scc1 .Lcqw_0p2_a
	s_waitcnt vmcnt(10)
	s_branch .Lcqw_0p2_b

; __device__ __forceinline__ void conv_queue(const P& p, LAS unsigned char* lds, int* ctr, int max_tiles) {
;     ...
;         CQ_PUT(2, 2); CQ_PUT(3, 3);
.Lcqw_0p2_b:
	v_cvt_pk_bf16_f32 v52, v2, v6
	s_cmp_eq_u32 s98, 0
	s_cbranch_scc1 .Lcqw_0p3_a
	s_waitcnt vmcnt(8)
	s_branch .Lcqw_0p3_b

; __device__ __forceinline__ void conv_queue(const P& p, LAS unsigned char* lds, int* ctr, int max_tiles) {
;     ...
;         CQ_PUT(2, 2); CQ_PUT(3, 3);
.Lcqw_0p3_b:
	v_cvt_pk_bf16_f32 v53, v10, v14
	v_cvt_pk_bf16_f32 v2, v3, v7
	v_cvt_pk_bf16_f32 v3, v11, v15
	ds_write2_b64 v84, v[52:53], v[2:3] offset0:24 offset1:57
	v_cvt_pk_bf16_f32 v2, v4, v8
	v_cvt_pk_bf16_f32 v3, v12, v16
	v_cvt_pk_bf16_f32 v4, v5, v9
	v_cvt_pk_bf16_f32 v5, v13, v17
	s_mov_b32 s6, 8
	s_movk_i32 s7, 0xff
	s_mov_b32 s11, 4
	s_mov_b32 s8, 15
	ds_write2_b64 v84, v[2:3], v[4:5] offset0:90 offset1:123
	s_branch .LBB0_846

; __device__ __forceinline__ void conv_queue(const P& p, LAS unsigned char* lds, int* ctr, int max_tiles) {
;     ...
;         CQ_PUT(2, 2); CQ_PUT(3, 3);
.LBB0_842:
	v_mov_b32_e32 v73, v19
	v_mov_b32_e32 v85, v19
	s_cmp_eq_u32 s98, 0
	s_cbranch_scc1 .Lcqw_0p4_a
	s_waitcnt vmcnt(14)
	s_branch .Lcqw_0p4_b

; __device__ __forceinline__ void conv_queue(const P& p, LAS unsigned char* lds, int* ctr, int max_tiles) {
;     ...
;         CQ_PUT(2, 2); CQ_PUT(3, 3);
.Lcqw_0p4_b:
	v_cvt_scalef32_pk_fp8_f32 v73, v52, v56, s23
	v_cvt_scalef32_pk_fp8_f32 v85, v53, v57, s23
	s_cmp_eq_u32 s98, 0
	s_cbranch_scc1 .Lcqw_0p5_a
	s_waitcnt vmcnt(12)
	s_branch .Lcqw_0p5_b

; __device__ __forceinline__ void conv_queue(const P& p, LAS unsigned char* lds, int* ctr, int max_tiles) {
;     ...
;         CQ_PUT(2, 2); CQ_PUT(3, 3);
.Lcqw_0p5_b:
	v_cvt_scalef32_pk_fp8_f32 v73, v60, v64, s23 op_sel:[0,0,0,1]
	v_cvt_scalef32_pk_fp8_f32 v85, v61, v65, s23 op_sel:[0,0,0,1]
	ds_write2_b32 v18, v73, v85 offset0:16 offset1:49
	v_mov_b32_e32 v73, v19
	v_mov_b32_e32 v85, v19
	v_cvt_scalef32_pk_fp8_f32 v73, v54, v58, s23
	v_cvt_scalef32_pk_fp8_f32 v85, v55, v59, s23
	v_cvt_scalef32_pk_fp8_f32 v73, v62, v66, s23 op_sel:[0,0,0,1]
	v_cvt_scalef32_pk_fp8_f32 v85, v63, v67, s23 op_sel:[0,0,0,1]
	ds_write2_b32 v18, v73, v85 offset0:82 offset1:115
	s_cbranch_execz .LBB0_838

; __device__ __forceinline__ void conv_queue(const P& p, LAS unsigned char* lds, int* ctr, int max_tiles) {
;     ...
;         CQ_PUT(2, 2); CQ_PUT(3, 3);
.LBB0_844:
	s_cmp_eq_u32 s98, 0
	s_cbranch_scc1 .Lcqw_0p6_a
	s_waitcnt vmcnt(15)
	s_branch .Lcqw_0p6_b

; __device__ __forceinline__ void conv_queue(const P& p, LAS unsigned char* lds, int* ctr, int max_tiles) {
;     ...
;         CQ_PUT(2, 2); CQ_PUT(3, 3);
.Lcqw_0p6_b:
	v_mov_b32_e32 v52, v19
	v_mov_b32_e32 v53, v19
	s_cmp_eq_u32 s98, 0
	s_cbranch_scc1 .Lcqw_0p7_a
	s_waitcnt vmcnt(10)
	s_branch .Lcqw_0p7_b

; __device__ __forceinline__ void conv_queue(const P& p, LAS unsigned char* lds, int* ctr, int max_tiles) {
;     ...
;         CQ_PUT(2, 2); CQ_PUT(3, 3);
.Lcqw_0p7_b:
	v_cvt_scalef32_pk_fp8_f32 v52, v2, v6, s23
	v_cvt_scalef32_pk_fp8_f32 v53, v3, v7, s23
	s_cmp_eq_u32 s98, 0
	s_cbranch_scc1 .Lcqw_0p8_a
	s_waitcnt vmcnt(8)
	s_branch .Lcqw_0p8_b

; __device__ __forceinline__ void conv_queue(const P& p, LAS unsigned char* lds, int* ctr, int max_tiles) {
;     ...
;         CQ_PUT(2, 2); CQ_PUT(3, 3);
.Lcqw_0p8_b:
	v_cvt_scalef32_pk_fp8_f32 v52, v10, v14, s23 op_sel:[0,0,0,1]
	v_cvt_scalef32_pk_fp8_f32 v53, v11, v15, s23 op_sel:[0,0,0,1]
	ds_write2_b32 v18, v52, v53 offset0:24 offset1:57
	v_mov_b32_e32 v52, v19
	v_mov_b32_e32 v53, v19
	v_cvt_scalef32_pk_fp8_f32 v52, v4, v8, s23
	v_cvt_scalef32_pk_fp8_f32 v53, v5, v9, s23
	v_cvt_scalef32_pk_fp8_f32 v52, v12, v16, s23 op_sel:[0,0,0,1]
	v_cvt_scalef32_pk_fp8_f32 v53, v13, v17, s23 op_sel:[0,0,0,1]
	ds_write2_b32 v18, v52, v53 offset0:90 offset1:123
	s_cbranch_execz .LBB0_840

; #define LAS __attribute__((address_space(3)))
; __device__ __forceinline__ void conv_queue(const P& p, LAS unsigned char* lds, int* ctr, int max_tiles) {
;     ...
;         __syncthreads();
;         { const int t2_ = cur_w1 ? t_cur : t_cur - NM1, e_ = cur_w1 ? t2_ >> 8 : t2_ >> 7, r_ = cur_w1 ? t2_ & 255 : t2_ & 127;
;           const int k0 = (cur_w1 ? r_ >> 4 : r_ >> 3) * 128, n0 = (cur_w1 ? r_ & 15 : r_ & 7) * 256;
;           if (cur_w1) {
;               unsigned char* Bt = p.ws + WS_W1_T + (size_t)e_ * 4096 * 2048;
; #pragma unroll 1
;               for (int ps = 0; ps < 2; ++ps) { const int id = tid + 512 * ps, n = id >> 2, q = id & 3; const LAS u32x2* tp_ = (const LAS u32x2*)(Tb + n * 264 + q * 64);
;                   u32x16 wv;
; #pragma unroll
;                   for (int i = 0; i < 8; ++i) { const u32x2 w = tp_[i]; wv[2 * i] = w.x; wv[2 * i + 1] = w.y; }
;                   u32x4 lo, hi; fp6_block_bf16(wv, lo, hi);
;                   unsigned char* dst = Bt + (size_t)DmW1{}(n0 + n) * 2048 + k0 + 16 * q;
;                   __builtin_nontemporal_store(lo, (u32x4*)dst); __builtin_nontemporal_store(hi, (u32x4*)(dst + 64)); }
;           } else {
;               unsigned char* Bt = p.ws + WS_W2_T + (size_t)e_ * 2048 * 2048;
; #pragma unroll
;               for (int ps = 0; ps < 4; ++ps) { const int n = ps * 64 + (tid >> 3), c = tid & 7; const LAS unsigned* tp_ = (const LAS unsigned*)(Tb + n * 132 + 16 * c);
;                   u32x4 w; w.x = tp_[0]; w.y = tp_[1]; w.z = tp_[2]; w.w = tp_[3];
;                   __builtin_nontemporal_store(w, (u32x4*)(Bt + (size_t)(n0 + n) * 2048 + k0 + 16 * c)); }
.LBB0_846:
	s_add_i32 s13, s26, 0xffffe000
	s_and_b64 s[16:17], exec, s[16:17]
	s_cselect_b32 s13, s26, s13
	s_and_b32 s7, s7, s13
	s_lshr_b32 s7, s7, s11
	s_ashr_i32 s6, s13, s6
	s_lshl_b32 s11, s7, 7
	s_and_b32 s7, s8, s13
	s_lshl_b32 s8, s7, 8
	s_ashr_i32 s7, s6, 31
	s_mov_b64 s[16:17], -1
	s_and_b64 vcc, exec, s[14:15]
	s_waitcnt lgkmcnt(0)
	s_barrier
	s_cbranch_vccz .LBB0_848
	s_lshl_b64 s[14:15], s[6:7], 22
	s_add_u32 s13, s3, s14
	v_add_u32_e32 v2, 0x4000, v81
	v_add_u32_e32 v4, 0x4008, v81
	s_addc_u32 s15, s20, s15
	ds_read2_b32 v[2:3], v2 offset1:1
	ds_read2_b32 v[4:5], v4 offset1:1
	s_add_u32 s14, s13, s11
	v_or_b32_e32 v6, s8, v76
	s_addc_u32 s15, s15, 0
	v_lshlrev_b32_e32 v18, 11, v6
	v_add_u32_e32 v6, 0x6100, v81
	v_add_u32_e32 v8, 0x6108, v81
	v_lshl_add_u64 v[10:11], s[14:15], 0, v[68:69]
	ds_read2_b32 v[6:7], v6 offset1:1
	ds_read2_b32 v[8:9], v8 offset1:1
	v_lshl_add_u64 v[12:13], v[10:11], 0, v[18:19]
	s_waitcnt lgkmcnt(2)
	global_store_dwordx4 v[12:13], v[2:5], off nt
	s_mov_b64 s[16:17], 0
	s_nop 0
	v_or_b32_e32 v2, s8, v78
	v_lshlrev_b32_e32 v18, 11, v2
	v_lshl_add_u64 v[2:3], v[10:11], 0, v[18:19]
	s_waitcnt lgkmcnt(0)
	global_store_dwordx4 v[2:3], v[6:9], off nt
	v_add_u32_e32 v2, 0x8200, v81
	v_add_u32_e32 v4, 0x8208, v81
	v_or_b32_e32 v6, s8, v79
	ds_read2_b32 v[2:3], v2 offset1:1
	ds_read2_b32 v[4:5], v4 offset1:1
	v_lshlrev_b32_e32 v18, 11, v6
	v_add_u32_e32 v6, 0xa300, v81
	v_add_u32_e32 v8, 0xa308, v81
	ds_read2_b32 v[6:7], v6 offset1:1
	ds_read2_b32 v[8:9], v8 offset1:1
	v_lshl_add_u64 v[12:13], v[10:11], 0, v[18:19]
	v_add_lshl_u32 v18, s8, v80, 11
	s_waitcnt lgkmcnt(2)
	global_store_dwordx4 v[12:13], v[2:5], off nt
	s_nop 1
	v_lshl_add_u64 v[2:3], v[10:11], 0, v[18:19]
	s_waitcnt lgkmcnt(0)
	global_store_dwordx4 v[2:3], v[6:9], off nt
.LBB0_848:
	s_andn2_b64 vcc, exec, s[16:17]
	s_cbranch_vccnz .LBB0_851
	s_lshl_b64 s[6:7], s[6:7], 23
	s_add_u32 s6, s21, s6
	s_addc_u32 s7, s22, s7
	s_add_u32 s6, s6, s11
	s_addc_u32 s7, s7, 0
	v_lshl_add_u64 v[52:53], s[6:7], 0, v[70:71]
	s_mov_b32 s11, 0
	s_mov_b64 s[6:7], -1

; #define CQ_LOAD(buf, slab, src, ldw) do { _Pragma("unroll") for (int r_ = 0; r_ < 4; ++r_) a[buf][r_] = __builtin_nontemporal_load((const f32x4*)(src + (size_t)((slab) * 32 + r_) * ldw)); } while (0)
; __device__ __forceinline__ void conv_queue(const P& p, LAS unsigned char* lds, int* ctr, int max_tiles) {
;     ...
;         __syncthreads();
;         if (!more) break;
;         CQ_LOAD(2, 2, s1, l1); CQ_LOAD(3, 3, s1, l1);
;         t_cur = t_nxt; t_nxt = qs[1 + (it & 1)];
.LBB0_851:
	s_and_b64 vcc, exec, s[4:5]
	s_mov_b64 s[4:5], -1
	s_barrier
	s_cbranch_vccnz .LBB0_817
	s_lshl_b32 s8, s10, 8
	v_lshl_add_u64 v[2:3], v[74:75], 0, s[8:9]
	s_lshl_b32 s8, s10, 2
	v_lshl_add_u64 v[4:5], v[2:3], 0, s[8:9]
	v_lshl_add_u64 v[6:7], v[4:5], 0, s[8:9]
	v_lshl_add_u64 v[8:9], v[6:7], 0, s[8:9]
	s_mov_b32 s13, s9
	v_lshl_add_u64 v[10:11], v[8:9], 0, s[12:13]
	s_and_b32 s4, s24, 1
	v_lshl_add_u64 v[12:13], v[10:11], 0, s[8:9]
	s_lshl_b32 s4, s4, 2
	v_lshl_add_u64 v[14:15], v[12:13], 0, s[8:9]
	s_add_i32 s4, s4, 0
	v_lshl_add_u64 v[16:17], v[14:15], 0, s[8:9]
	s_add_i32 s11, s4, 0x16464
	s_add_i32 s24, s24, 1
	s_mov_b64 s[4:5], 0
	s_branch .LBB0_817
